# speedup vs baseline: 1.0050x; 1.0050x over previous
.Lk1_nowarm9:
	buffer_load_dword v8, v1, s[8:11], s40 offen nt
	buffer_load_dword v9, v1, s[8:11], s41 offen nt
	buffer_load_dword v10, v1, s[8:11], s42 offen nt
	buffer_load_dword v11, v1, s[8:11], s43 offen nt
	buffer_load_dword v12, v1, s[8:11], s44 offen nt
	buffer_load_dword v13, v1, s[8:11], s45 offen nt
	buffer_load_dword v14, v1, s[8:11], s46 offen nt
	buffer_load_dword v15, v1, s[8:11], s47 offen nt
	buffer_load_dword v16, v1, s[8:11], s48 offen nt
	buffer_load_dword v17, v1, s[8:11], s49 offen nt
	buffer_load_dword v18, v1, s[8:11], s50 offen nt
	buffer_load_dword v19, v1, s[8:11], s51 offen nt
	buffer_load_dword v20, v1, s[8:11], s52 offen nt
	buffer_load_dword v21, v1, s[8:11], s53 offen nt
	buffer_load_dword v22, v1, s[8:11], s54 offen nt
	buffer_load_dword v23, v1, s[8:11], s55 offen nt
	s_add_u32 s8, s8, 0x4e200
	s_addc_u32 s9, s9, 0
	buffer_load_dword v24, v1, s[8:11], s40 offen nt
	buffer_load_dword v25, v1, s[8:11], s41 offen nt
	buffer_load_dword v26, v1, s[8:11], s42 offen nt
	buffer_load_dword v27, v1, s[8:11], s43 offen nt
	buffer_load_dword v28, v1, s[8:11], s44 offen nt
	buffer_load_dword v29, v1, s[8:11], s45 offen nt
	buffer_load_dword v30, v1, s[8:11], s46 offen nt
	buffer_load_dword v31, v1, s[8:11], s47 offen nt
	buffer_load_dword v32, v1, s[8:11], s48 offen nt
	buffer_load_dword v33, v1, s[8:11], s49 offen nt
	buffer_load_dword v34, v1, s[8:11], s50 offen nt
	buffer_load_dword v35, v1, s[8:11], s51 offen nt
	buffer_load_dword v36, v1, s[8:11], s52 offen nt
	buffer_load_dword v37, v1, s[8:11], s53 offen nt
	buffer_load_dword v38, v1, s[8:11], s54 offen nt
	buffer_load_dword v39, v1, s[8:11], s55 offen nt
	s_add_u32 s8, s8, 0x4e200
	s_addc_u32 s9, s9, 0
	buffer_load_dword v40, v1, s[8:11], s40 offen nt
	buffer_load_dword v41, v1, s[8:11], s41 offen nt
	buffer_load_dword v42, v1, s[8:11], s42 offen nt
	buffer_load_dword v43, v1, s[8:11], s43 offen nt
	buffer_load_dword v44, v1, s[8:11], s44 offen nt
	buffer_load_dword v45, v1, s[8:11], s45 offen nt
	buffer_load_dword v46, v1, s[8:11], s46 offen nt
	buffer_load_dword v47, v1, s[8:11], s47 offen nt
	buffer_load_dword v48, v1, s[8:11], s48 offen nt
	buffer_load_dword v49, v1, s[8:11], s49 offen nt
	buffer_load_dword v50, v1, s[8:11], s50 offen nt
	buffer_load_dword v51, v1, s[8:11], s51 offen nt
	buffer_load_dword v52, v1, s[8:11], s52 offen nt
	buffer_load_dword v53, v1, s[8:11], s53 offen nt
	buffer_load_dword v54, v1, s[8:11], s54 offen nt
	buffer_load_dword v55, v1, s[8:11], s55 offen nt
	v_mul_u32_u24_e32 v3, 0x147b, v2
	v_lshrrev_b32_e32 v3, 19, v3
	v_mul_u32_u24_e32 v98, 0x64, v3
	v_sub_u32_e32 v98, v2, v98
	v_add_u32_e32 v3, -1, v3
	v_add_u32_e32 v98, -1, v98
	s_movk_i32 s17, 0x62
	v_cmp_gt_u32_e64 s[36:37], 48, v3
	v_cmp_gt_u32_e64 s[38:39], s17, v98
	s_mul_i32 s17, s15, 0x1388
	v_add_lshl_u32 v98, v2, s17, 3
	s_and_b64 s[36:37], s[36:37], s[38:39]
	s_waitcnt vmcnt(32)
	s_add_u32 s8, s8, 0x4e200
	s_addc_u32 s9, s9, 0
	buffer_load_dword v56, v1, s[8:11], s40 offen nt
	buffer_load_dword v57, v1, s[8:11], s41 offen nt
	buffer_load_dword v58, v1, s[8:11], s42 offen nt
	buffer_load_dword v59, v1, s[8:11], s43 offen nt
	buffer_load_dword v60, v1, s[8:11], s44 offen nt
	buffer_load_dword v61, v1, s[8:11], s45 offen nt
	buffer_load_dword v62, v1, s[8:11], s46 offen nt
	buffer_load_dword v63, v1, s[8:11], s47 offen nt
	buffer_load_dword v64, v1, s[8:11], s48 offen nt
	buffer_load_dword v65, v1, s[8:11], s49 offen nt
	buffer_load_dword v66, v1, s[8:11], s50 offen nt
	buffer_load_dword v67, v1, s[8:11], s51 offen nt
	buffer_load_dword v68, v1, s[8:11], s52 offen nt
	buffer_load_dword v69, v1, s[8:11], s53 offen nt
	buffer_load_dword v70, v1, s[8:11], s54 offen nt
	buffer_load_dword v71, v1, s[8:11], s55 offen nt
	s_add_u32 s8, s8, 0x4e200
	s_addc_u32 s9, s9, 0
	buffer_load_dword v72, v1, s[8:11], s40 offen nt
	v_max3_f32 v76, v8, v9, v10
	v_max3_f32 v76, v76, v11, v12
	v_max3_f32 v76, v76, v13, v14
	v_max3_f32 v76, v76, v15, v16
	v_max3_f32 v76, v76, v17, v18
	v_max3_f32 v76, v76, v19, v20
	v_max3_f32 v76, v76, v21, v22
	v_max_f32_e32 v76, v76, v23
	v_sub_f32_e32 v8, v8, v76
	v_sub_f32_e32 v9, v9, v76
	v_sub_f32_e32 v10, v10, v76
	v_sub_f32_e32 v11, v11, v76
	v_sub_f32_e32 v12, v12, v76
	v_sub_f32_e32 v13, v13, v76
	v_sub_f32_e32 v14, v14, v76
	v_sub_f32_e32 v15, v15, v76
	v_sub_f32_e32 v16, v16, v76
	v_sub_f32_e32 v17, v17, v76
	v_sub_f32_e32 v18, v18, v76
	v_sub_f32_e32 v19, v19, v76
	v_sub_f32_e32 v20, v20, v76
	v_sub_f32_e32 v21, v21, v76
	v_sub_f32_e32 v22, v22, v76
	v_sub_f32_e32 v23, v23, v76
	v_or_b32_e32 v81, 0, v8
	v_or_b32_e32 v82, 1, v9
	v_min_u32_e32 v80, v81, v82
	v_or_b32_e32 v81, 2, v10
	v_or_b32_e32 v82, 3, v11
	v_min3_u32 v80, v80, v81, v82
	v_or_b32_e32 v81, 4, v12
	v_or_b32_e32 v82, 5, v13
	v_min3_u32 v80, v80, v81, v82
	v_or_b32_e32 v81, 6, v14
	v_or_b32_e32 v82, 7, v15
	v_min3_u32 v80, v80, v81, v82
	v_or_b32_e32 v81, 8, v16
	v_or_b32_e32 v82, 9, v17
	v_min3_u32 v80, v80, v81, v82
	v_or_b32_e32 v81, 10, v18
	v_or_b32_e32 v82, 11, v19
	v_min3_u32 v80, v80, v81, v82
	v_or_b32_e32 v81, 12, v20
	v_or_b32_e32 v82, 13, v21
	v_min3_u32 v80, v80, v81, v82
	v_or_b32_e32 v81, 14, v22
	v_or_b32_e32 v82, 15, v23
	v_min3_u32 v80, v80, v81, v82
	v_mul_f32_e32 v8, s14, v8
	v_mul_f32_e32 v9, s14, v9
	v_mul_f32_e32 v10, s14, v10
	v_mul_f32_e32 v11, s14, v11
	v_mul_f32_e32 v12, s14, v12
	v_mul_f32_e32 v13, s14, v13
	v_mul_f32_e32 v14, s14, v14
	v_mul_f32_e32 v15, s14, v15
	v_mul_f32_e32 v16, s14, v16
	v_mul_f32_e32 v17, s14, v17
	v_mul_f32_e32 v18, s14, v18
	v_mul_f32_e32 v19, s14, v19
	v_mul_f32_e32 v20, s14, v20
	v_mul_f32_e32 v21, s14, v21
	v_mul_f32_e32 v22, s14, v22
	v_mul_f32_e32 v23, s14, v23
	v_exp_f32_e32 v8, v8
	v_exp_f32_e32 v9, v9
	v_exp_f32_e32 v10, v10
	v_exp_f32_e32 v11, v11
	v_exp_f32_e32 v12, v12
	v_exp_f32_e32 v13, v13
	v_exp_f32_e32 v14, v14
	v_exp_f32_e32 v15, v15
	v_exp_f32_e32 v16, v16
	v_exp_f32_e32 v17, v17
	v_exp_f32_e32 v18, v18
	v_exp_f32_e32 v19, v19
	v_exp_f32_e32 v20, v20
	v_exp_f32_e32 v21, v21
	v_exp_f32_e32 v22, v22
	v_exp_f32_e32 v23, v23
	v_add_f32_e32 v78, v8, v10
	v_add_f32_e32 v79, v9, v11
	v_add_f32_e32 v78, v78, v12
	v_add_f32_e32 v79, v79, v13
	v_add_f32_e32 v78, v78, v14
	v_add_f32_e32 v79, v79, v15
	v_add_f32_e32 v78, v78, v16
	v_add_f32_e32 v79, v79, v17
	v_add_f32_e32 v78, v78, v18
	v_add_f32_e32 v79, v79, v19
	v_add_f32_e32 v78, v78, v20
	v_add_f32_e32 v79, v79, v21
	v_add_f32_e32 v78, v78, v22
	v_add_f32_e32 v79, v79, v23
	v_add_f32_e32 v78, v78, v79
	v_cvt_f64_f32_e32 v[86:87], v78
	v_mov_b32_e32 v75, v80
	v_mov_b32_e32 v73, v76
	s_waitcnt vmcnt(33)
	v_max3_f32 v76, v24, v25, v26
	v_max3_f32 v76, v76, v27, v28
	v_max3_f32 v76, v76, v29, v30
	v_max3_f32 v76, v76, v31, v32
	v_max3_f32 v76, v76, v33, v34
	v_max3_f32 v76, v76, v35, v36
	v_max3_f32 v76, v76, v37, v38
	v_max_f32_e32 v76, v76, v39
	v_max_f32_e32 v77, v73, v76
	v_cmp_gt_f32_e64 s[26:27], v76, v73
	v_sub_f32_e32 v83, v73, v77
	v_mul_f32_e32 v83, s14, v83
	v_exp_f32_e32 v83, v83
	v_sub_f32_e32 v24, v24, v77
	v_sub_f32_e32 v25, v25, v77
	v_sub_f32_e32 v26, v26, v77
	v_sub_f32_e32 v27, v27, v77
	v_sub_f32_e32 v28, v28, v77
	v_sub_f32_e32 v29, v29, v77
	v_sub_f32_e32 v30, v30, v77
	v_sub_f32_e32 v31, v31, v77
	v_sub_f32_e32 v32, v32, v77
	v_sub_f32_e32 v33, v33, v77
	v_sub_f32_e32 v34, v34, v77
	v_sub_f32_e32 v35, v35, v77
	v_sub_f32_e32 v36, v36, v77
	v_sub_f32_e32 v37, v37, v77
	v_sub_f32_e32 v38, v38, v77
	v_sub_f32_e32 v39, v39, v77
	v_cvt_f64_f32_e32 v[84:85], v83
	v_or_b32_e32 v81, 16, v24
	v_or_b32_e32 v82, 17, v25
	v_min_u32_e32 v80, v81, v82
	v_or_b32_e32 v81, 18, v26
	v_or_b32_e32 v82, 19, v27
	v_min3_u32 v80, v80, v81, v82
	v_or_b32_e32 v81, 20, v28
	v_or_b32_e32 v82, 21, v29
	v_min3_u32 v80, v80, v81, v82
	v_or_b32_e32 v81, 22, v30
	v_or_b32_e32 v82, 23, v31
	v_min3_u32 v80, v80, v81, v82
	v_or_b32_e32 v81, 24, v32
	v_or_b32_e32 v82, 25, v33
	v_min3_u32 v80, v80, v81, v82
	v_or_b32_e32 v81, 26, v34
	v_or_b32_e32 v82, 27, v35
	v_min3_u32 v80, v80, v81, v82
	v_or_b32_e32 v81, 28, v36
	v_or_b32_e32 v82, 29, v37
	v_min3_u32 v80, v80, v81, v82
	v_or_b32_e32 v81, 30, v38
	v_or_b32_e32 v82, 31, v39
	v_min3_u32 v80, v80, v81, v82
	v_mul_f64 v[86:87], v[86:87], v[84:85]
	v_mul_f32_e32 v24, s14, v24
	v_mul_f32_e32 v25, s14, v25
	v_mul_f32_e32 v26, s14, v26
	v_mul_f32_e32 v27, s14, v27
	v_mul_f32_e32 v28, s14, v28
	v_mul_f32_e32 v29, s14, v29
	v_mul_f32_e32 v30, s14, v30
	v_mul_f32_e32 v31, s14, v31
	v_mul_f32_e32 v32, s14, v32
	v_mul_f32_e32 v33, s14, v33
	v_mul_f32_e32 v34, s14, v34
	v_mul_f32_e32 v35, s14, v35
	v_mul_f32_e32 v36, s14, v36
	v_mul_f32_e32 v37, s14, v37
	v_mul_f32_e32 v38, s14, v38
	v_mul_f32_e32 v39, s14, v39
	v_exp_f32_e32 v24, v24
	v_exp_f32_e32 v25, v25
	v_exp_f32_e32 v26, v26
	v_exp_f32_e32 v27, v27
	v_exp_f32_e32 v28, v28
	v_exp_f32_e32 v29, v29
	v_exp_f32_e32 v30, v30
	v_exp_f32_e32 v31, v31
	v_exp_f32_e32 v32, v32
	v_exp_f32_e32 v33, v33
	v_exp_f32_e32 v34, v34
	v_exp_f32_e32 v35, v35
	v_exp_f32_e32 v36, v36
	v_exp_f32_e32 v37, v37
	v_exp_f32_e32 v38, v38
	v_exp_f32_e32 v39, v39
	v_add_f32_e32 v78, v24, v26
	v_add_f32_e32 v79, v25, v27
	v_add_f32_e32 v78, v78, v28
	v_add_f32_e32 v79, v79, v29
	v_add_f32_e32 v78, v78, v30
	v_add_f32_e32 v79, v79, v31
	v_add_f32_e32 v78, v78, v32
	v_add_f32_e32 v79, v79, v33
	v_add_f32_e32 v78, v78, v34
	v_add_f32_e32 v79, v79, v35
	v_add_f32_e32 v78, v78, v36
	v_add_f32_e32 v79, v79, v37
	v_add_f32_e32 v78, v78, v38
	v_add_f32_e32 v79, v79, v39
	v_add_f32_e32 v78, v78, v79
	v_cvt_f64_f32_e32 v[84:85], v78
	v_cndmask_b32_e64 v75, v75, v80, s[26:27]
	v_mov_b32_e32 v73, v77
	v_add_f64 v[86:87], v[86:87], v[84:85]
	s_waitcnt vmcnt(17)
	v_max3_f32 v76, v40, v41, v42
	v_max3_f32 v76, v76, v43, v44
	v_max3_f32 v76, v76, v45, v46
	v_max3_f32 v76, v76, v47, v48
	v_max3_f32 v76, v76, v49, v50
	v_max3_f32 v76, v76, v51, v52
	v_max3_f32 v76, v76, v53, v54
	v_max_f32_e32 v76, v76, v55
	v_max_f32_e32 v77, v73, v76
	v_cmp_gt_f32_e64 s[26:27], v76, v73
	v_sub_f32_e32 v83, v73, v77
	v_mul_f32_e32 v83, s14, v83
	v_exp_f32_e32 v83, v83
	v_sub_f32_e32 v40, v40, v77
	v_sub_f32_e32 v41, v41, v77
	v_sub_f32_e32 v42, v42, v77
	v_sub_f32_e32 v43, v43, v77
	v_sub_f32_e32 v44, v44, v77
	v_sub_f32_e32 v45, v45, v77
	v_sub_f32_e32 v46, v46, v77
	v_sub_f32_e32 v47, v47, v77
	v_sub_f32_e32 v48, v48, v77
	v_sub_f32_e32 v49, v49, v77
	v_sub_f32_e32 v50, v50, v77
	v_sub_f32_e32 v51, v51, v77
	v_sub_f32_e32 v52, v52, v77
	v_sub_f32_e32 v53, v53, v77
	v_sub_f32_e32 v54, v54, v77
	v_sub_f32_e32 v55, v55, v77
	v_cvt_f64_f32_e32 v[84:85], v83
	v_or_b32_e32 v81, 32, v40
	v_or_b32_e32 v82, 33, v41
	v_min_u32_e32 v80, v81, v82
	v_or_b32_e32 v81, 34, v42
	v_or_b32_e32 v82, 35, v43
	v_min3_u32 v80, v80, v81, v82
	v_or_b32_e32 v81, 36, v44
	v_or_b32_e32 v82, 37, v45
	v_min3_u32 v80, v80, v81, v82
	v_or_b32_e32 v81, 38, v46
	v_or_b32_e32 v82, 39, v47
	v_min3_u32 v80, v80, v81, v82
	v_or_b32_e32 v81, 40, v48
	v_or_b32_e32 v82, 41, v49
	v_min3_u32 v80, v80, v81, v82
	v_or_b32_e32 v81, 42, v50
	v_or_b32_e32 v82, 43, v51
	v_min3_u32 v80, v80, v81, v82
	v_or_b32_e32 v81, 44, v52
	v_or_b32_e32 v82, 45, v53
	v_min3_u32 v80, v80, v81, v82
	v_or_b32_e32 v81, 46, v54
	v_or_b32_e32 v82, 47, v55
	v_min3_u32 v80, v80, v81, v82
	v_mul_f64 v[86:87], v[86:87], v[84:85]
	v_mul_f32_e32 v40, s14, v40
	v_mul_f32_e32 v41, s14, v41
	v_mul_f32_e32 v42, s14, v42
	v_mul_f32_e32 v43, s14, v43
	v_mul_f32_e32 v44, s14, v44
	v_mul_f32_e32 v45, s14, v45
	v_mul_f32_e32 v46, s14, v46
	v_mul_f32_e32 v47, s14, v47
	v_mul_f32_e32 v48, s14, v48
	v_mul_f32_e32 v49, s14, v49
	v_mul_f32_e32 v50, s14, v50
	v_mul_f32_e32 v51, s14, v51
	v_mul_f32_e32 v52, s14, v52
	v_mul_f32_e32 v53, s14, v53
	v_mul_f32_e32 v54, s14, v54
	v_mul_f32_e32 v55, s14, v55
	v_exp_f32_e32 v40, v40
	v_exp_f32_e32 v41, v41
	v_exp_f32_e32 v42, v42
	v_exp_f32_e32 v43, v43
	v_exp_f32_e32 v44, v44
	v_exp_f32_e32 v45, v45
	v_exp_f32_e32 v46, v46
	v_exp_f32_e32 v47, v47
	v_exp_f32_e32 v48, v48
	v_exp_f32_e32 v49, v49
	v_exp_f32_e32 v50, v50
	v_exp_f32_e32 v51, v51
	v_exp_f32_e32 v52, v52
	v_exp_f32_e32 v53, v53
	v_exp_f32_e32 v54, v54
	v_exp_f32_e32 v55, v55
	v_add_f32_e32 v78, v40, v42
	v_add_f32_e32 v79, v41, v43
	v_add_f32_e32 v78, v78, v44
	v_add_f32_e32 v79, v79, v45
	v_add_f32_e32 v78, v78, v46
	v_add_f32_e32 v79, v79, v47
	v_add_f32_e32 v78, v78, v48
	v_add_f32_e32 v79, v79, v49
	v_add_f32_e32 v78, v78, v50
	v_add_f32_e32 v79, v79, v51
	v_add_f32_e32 v78, v78, v52
	v_add_f32_e32 v79, v79, v53
	v_add_f32_e32 v78, v78, v54
	v_add_f32_e32 v79, v79, v55
	v_add_f32_e32 v78, v78, v79
	v_cvt_f64_f32_e32 v[84:85], v78
	v_cndmask_b32_e64 v75, v75, v80, s[26:27]
	v_mov_b32_e32 v73, v77
	v_add_f64 v[86:87], v[86:87], v[84:85]
	s_waitcnt vmcnt(9)
	v_max3_f32 v76, v56, v57, v58
	v_max3_f32 v76, v76, v59, v60
	v_max3_f32 v76, v76, v61, v62
	v_max_f32_e32 v76, v76, v63
	v_max_f32_e32 v77, v73, v76
	v_cmp_gt_f32_e64 s[26:27], v76, v73
	v_sub_f32_e32 v83, v73, v77
	v_mul_f32_e32 v83, s14, v83
	v_exp_f32_e32 v83, v83
	v_sub_f32_e32 v56, v56, v77
	v_sub_f32_e32 v57, v57, v77
	v_sub_f32_e32 v58, v58, v77
	v_sub_f32_e32 v59, v59, v77
	v_sub_f32_e32 v60, v60, v77
	v_sub_f32_e32 v61, v61, v77
	v_sub_f32_e32 v62, v62, v77
	v_sub_f32_e32 v63, v63, v77
	v_cvt_f64_f32_e32 v[84:85], v83
	v_or_b32_e32 v81, 48, v56
	v_or_b32_e32 v82, 49, v57
	v_min_u32_e32 v80, v81, v82
	v_or_b32_e32 v81, 50, v58
	v_or_b32_e32 v82, 51, v59
	v_min3_u32 v80, v80, v81, v82
	v_or_b32_e32 v81, 52, v60
	v_or_b32_e32 v82, 53, v61
	v_min3_u32 v80, v80, v81, v82
	v_or_b32_e32 v81, 54, v62
	v_or_b32_e32 v82, 55, v63
	v_min3_u32 v80, v80, v81, v82
	v_mul_f64 v[86:87], v[86:87], v[84:85]
	v_mul_f32_e32 v56, s14, v56
	v_mul_f32_e32 v57, s14, v57
	v_mul_f32_e32 v58, s14, v58
	v_mul_f32_e32 v59, s14, v59
	v_mul_f32_e32 v60, s14, v60
	v_mul_f32_e32 v61, s14, v61
	v_mul_f32_e32 v62, s14, v62
	v_mul_f32_e32 v63, s14, v63
	v_exp_f32_e32 v56, v56
	v_exp_f32_e32 v57, v57
	v_exp_f32_e32 v58, v58
	v_exp_f32_e32 v59, v59
	v_exp_f32_e32 v60, v60
	v_exp_f32_e32 v61, v61
	v_exp_f32_e32 v62, v62
	v_exp_f32_e32 v63, v63
	v_add_f32_e32 v78, v56, v58
	v_add_f32_e32 v79, v57, v59
	v_add_f32_e32 v78, v78, v60
	v_add_f32_e32 v79, v79, v61
	v_add_f32_e32 v78, v78, v62
	v_add_f32_e32 v79, v79, v63
	v_add_f32_e32 v78, v78, v79
	v_cvt_f64_f32_e32 v[84:85], v78
	v_cndmask_b32_e64 v75, v75, v80, s[26:27]
	v_mov_b32_e32 v73, v77
	v_add_f64 v[86:87], v[86:87], v[84:85]
	s_waitcnt vmcnt(5)
	v_max3_f32 v76, v64, v65, v66
	v_max_f32_e32 v76, v76, v67
	v_max_f32_e32 v77, v73, v76
	v_cmp_gt_f32_e64 s[26:27], v76, v73
	v_sub_f32_e32 v83, v73, v77
	v_mul_f32_e32 v83, s14, v83
	v_exp_f32_e32 v83, v83
	v_sub_f32_e32 v64, v64, v77
	v_sub_f32_e32 v65, v65, v77
	v_sub_f32_e32 v66, v66, v77
	v_sub_f32_e32 v67, v67, v77
	v_cvt_f64_f32_e32 v[84:85], v83
	v_or_b32_e32 v81, 56, v64
	v_or_b32_e32 v82, 57, v65
	v_min_u32_e32 v80, v81, v82
	v_or_b32_e32 v81, 58, v66
	v_or_b32_e32 v82, 59, v67
	v_min3_u32 v80, v80, v81, v82
	v_mul_f64 v[86:87], v[86:87], v[84:85]
	v_mul_f32_e32 v64, s14, v64
	v_mul_f32_e32 v65, s14, v65
	v_mul_f32_e32 v66, s14, v66
	v_mul_f32_e32 v67, s14, v67
	v_exp_f32_e32 v64, v64
	v_exp_f32_e32 v65, v65
	v_exp_f32_e32 v66, v66
	v_exp_f32_e32 v67, v67
	v_add_f32_e32 v78, v64, v66
	v_add_f32_e32 v79, v65, v67
	v_add_f32_e32 v78, v78, v79
	v_cvt_f64_f32_e32 v[84:85], v78
	v_cndmask_b32_e64 v75, v75, v80, s[26:27]
	v_mov_b32_e32 v73, v77
	v_add_f64 v[86:87], v[86:87], v[84:85]
	s_waitcnt vmcnt(4)
	v_max_f32_e32 v77, v73, v68
	v_cmp_gt_f32_e64 s[26:27], v68, v73
	v_sub_f32_e32 v83, v73, v77
	v_sub_f32_e32 v68, v68, v77
	v_mul_f32_e32 v83, s14, v83
	v_mul_f32_e32 v68, s14, v68
	v_exp_f32_e32 v83, v83
	v_exp_f32_e32 v68, v68
	v_cndmask_b32_e64 v75, v75, 60, s[26:27]
	v_cvt_f64_f32_e32 v[84:85], v83
	v_cvt_f64_f32_e32 v[90:91], v68
	v_mul_f64 v[86:87], v[86:87], v[84:85]
	v_mov_b32_e32 v73, v77
	v_add_f64 v[86:87], v[86:87], v[90:91]
	s_waitcnt vmcnt(3)
	v_max_f32_e32 v77, v73, v69
	v_cmp_gt_f32_e64 s[26:27], v69, v73
	v_sub_f32_e32 v83, v73, v77
	v_sub_f32_e32 v69, v69, v77
	v_mul_f32_e32 v83, s14, v83
	v_mul_f32_e32 v69, s14, v69
	v_exp_f32_e32 v83, v83
	v_exp_f32_e32 v69, v69
	v_cndmask_b32_e64 v75, v75, 61, s[26:27]
	v_cvt_f64_f32_e32 v[84:85], v83
	v_cvt_f64_f32_e32 v[90:91], v69
	v_mul_f64 v[86:87], v[86:87], v[84:85]
	v_mov_b32_e32 v73, v77
	v_add_f64 v[86:87], v[86:87], v[90:91]
	s_waitcnt vmcnt(2)
	v_max_f32_e32 v77, v73, v70
	v_cmp_gt_f32_e64 s[26:27], v70, v73
	v_sub_f32_e32 v83, v73, v77
	v_sub_f32_e32 v70, v70, v77
	v_mul_f32_e32 v83, s14, v83
	v_mul_f32_e32 v70, s14, v70
	v_exp_f32_e32 v83, v83
	v_exp_f32_e32 v70, v70
	v_cndmask_b32_e64 v75, v75, 62, s[26:27]
	v_cvt_f64_f32_e32 v[84:85], v83
	v_cvt_f64_f32_e32 v[90:91], v70
	v_mul_f64 v[86:87], v[86:87], v[84:85]
	v_mov_b32_e32 v73, v77
	v_add_f64 v[86:87], v[86:87], v[90:91]
	s_waitcnt vmcnt(1)
	v_max_f32_e32 v77, v73, v71
	v_cmp_gt_f32_e64 s[26:27], v71, v73
	v_sub_f32_e32 v83, v73, v77
	v_sub_f32_e32 v71, v71, v77
	v_mul_f32_e32 v83, s14, v83
	v_mul_f32_e32 v71, s14, v71
	v_exp_f32_e32 v83, v83
	v_exp_f32_e32 v71, v71
	v_cndmask_b32_e64 v75, v75, 63, s[26:27]
	v_cvt_f64_f32_e32 v[84:85], v83
	v_cvt_f64_f32_e32 v[90:91], v71
	v_mul_f64 v[86:87], v[86:87], v[84:85]
	v_mov_b32_e32 v73, v77
	v_add_f64 v[86:87], v[86:87], v[90:91]
	s_waitcnt vmcnt(0)
	v_max_f32_e32 v77, v73, v72
	v_cmp_gt_f32_e64 s[26:27], v72, v73
	v_sub_f32_e32 v83, v73, v77
	v_sub_f32_e32 v72, v72, v77
	v_mul_f32_e32 v83, s14, v83
	v_mul_f32_e32 v72, s14, v72
	v_exp_f32_e32 v83, v83
	v_exp_f32_e32 v72, v72
	v_cndmask_b32_e64 v75, v75, 64, s[26:27]
	v_cvt_f64_f32_e32 v[84:85], v83
	v_cvt_f64_f32_e32 v[90:91], v72
	v_mul_f64 v[86:87], v[86:87], v[84:85]
	v_add_f64 v[86:87], v[86:87], v[90:91]
	v_rcp_f64_e32 v[88:89], v[86:87]
	v_cmp_gt_u32_e32 vcc, 64, v75
	s_and_b64 vcc, vcc, s[36:37]
	v_fma_f64 v[90:91], -v[86:87], v[88:89], 1.0
	v_fma_f64 v[88:89], v[90:91], v[88:89], v[88:89]
	v_cvt_f32_f64_e32 v3, v[88:89]
	v_cndmask_b32_e32 v74, 0, v3, vcc
	global_store_dwordx2 v98, v[74:75], s[6:7]
